# v32 + P0 silu table: 12 loads issued together; route phase: norm gain/shift/scale (24 dwordx4 per lane) loaded once per workgroup pass instead of per row (8 dependent L2 round trips per row removed)
# speedup vs baseline: 1.0055x; 1.0055x over previous
; __device__ __forceinline__ float silu_f(float x) { return x / (1.0f + __expf(-x)); }
; __device__ __forceinline__ void adaln_item(Frame& F, const float* wmod, const float* bmod, float* mod, int slab) {
;     ...
;     for (int i = F.tid; i < 3 * DM; i += NWAVES * 64) { const float x = i < 2 * DM ? c[i] : cc[i - 2 * DM]; sl[i] = silu_f(x); }
.LBB0_12:
	s_movk_i32 s4, 0x1000
	v_cmp_gt_u32_e32 vcc, s4, v7
	v_add_u32_e32 v10, 0x200, v7
	s_nop 0
	v_cndmask_b32_e32 v9, v5, v3, vcc
	v_cndmask_b32_e32 v8, v4, v2, vcc
	global_load_dword v200, v[8:9], off
	v_mov_b32_e32 v7, v10
	v_lshl_add_u64 v[4:5], v[4:5], 0, s[36:37]
	v_lshl_add_u64 v[2:3], v[2:3], 0, s[36:37]
	v_cmp_gt_u32_e32 vcc, s4, v7
	v_add_u32_e32 v10, 0x200, v7
	s_nop 0
	v_cndmask_b32_e32 v9, v5, v3, vcc
	v_cndmask_b32_e32 v8, v4, v2, vcc
	global_load_dword v201, v[8:9], off
	v_mov_b32_e32 v7, v10
	v_lshl_add_u64 v[4:5], v[4:5], 0, s[36:37]
	v_lshl_add_u64 v[2:3], v[2:3], 0, s[36:37]
	v_cmp_gt_u32_e32 vcc, s4, v7
	v_add_u32_e32 v10, 0x200, v7
	s_nop 0
	v_cndmask_b32_e32 v9, v5, v3, vcc
	v_cndmask_b32_e32 v8, v4, v2, vcc
	global_load_dword v202, v[8:9], off
	v_mov_b32_e32 v7, v10
	v_lshl_add_u64 v[4:5], v[4:5], 0, s[36:37]
	v_lshl_add_u64 v[2:3], v[2:3], 0, s[36:37]
	v_cmp_gt_u32_e32 vcc, s4, v7
	v_add_u32_e32 v10, 0x200, v7
	s_nop 0
	v_cndmask_b32_e32 v9, v5, v3, vcc
	v_cndmask_b32_e32 v8, v4, v2, vcc
	global_load_dword v203, v[8:9], off
	v_mov_b32_e32 v7, v10
	v_lshl_add_u64 v[4:5], v[4:5], 0, s[36:37]
	v_lshl_add_u64 v[2:3], v[2:3], 0, s[36:37]
	v_cmp_gt_u32_e32 vcc, s4, v7
	v_add_u32_e32 v10, 0x200, v7
	s_nop 0
	v_cndmask_b32_e32 v9, v5, v3, vcc
	v_cndmask_b32_e32 v8, v4, v2, vcc
	global_load_dword v204, v[8:9], off
	v_mov_b32_e32 v7, v10
	v_lshl_add_u64 v[4:5], v[4:5], 0, s[36:37]
	v_lshl_add_u64 v[2:3], v[2:3], 0, s[36:37]
	v_cmp_gt_u32_e32 vcc, s4, v7
	v_add_u32_e32 v10, 0x200, v7
	s_nop 0
	v_cndmask_b32_e32 v9, v5, v3, vcc
	v_cndmask_b32_e32 v8, v4, v2, vcc
	global_load_dword v205, v[8:9], off
	v_mov_b32_e32 v7, v10
	v_lshl_add_u64 v[4:5], v[4:5], 0, s[36:37]
	v_lshl_add_u64 v[2:3], v[2:3], 0, s[36:37]
	v_cmp_gt_u32_e32 vcc, s4, v7
	v_add_u32_e32 v10, 0x200, v7
	s_nop 0
	v_cndmask_b32_e32 v9, v5, v3, vcc
	v_cndmask_b32_e32 v8, v4, v2, vcc
	global_load_dword v206, v[8:9], off
	v_mov_b32_e32 v7, v10
	v_lshl_add_u64 v[4:5], v[4:5], 0, s[36:37]
	v_lshl_add_u64 v[2:3], v[2:3], 0, s[36:37]
	v_cmp_gt_u32_e32 vcc, s4, v7
	v_add_u32_e32 v10, 0x200, v7
	s_nop 0
	v_cndmask_b32_e32 v9, v5, v3, vcc
	v_cndmask_b32_e32 v8, v4, v2, vcc
	global_load_dword v207, v[8:9], off
	v_mov_b32_e32 v7, v10
	v_lshl_add_u64 v[4:5], v[4:5], 0, s[36:37]
	v_lshl_add_u64 v[2:3], v[2:3], 0, s[36:37]
	v_cmp_gt_u32_e32 vcc, s4, v7
	v_add_u32_e32 v10, 0x200, v7
	s_nop 0
	v_cndmask_b32_e32 v9, v5, v3, vcc
	v_cndmask_b32_e32 v8, v4, v2, vcc
	global_load_dword v208, v[8:9], off
	v_mov_b32_e32 v7, v10
	v_lshl_add_u64 v[4:5], v[4:5], 0, s[36:37]
	v_lshl_add_u64 v[2:3], v[2:3], 0, s[36:37]
	v_cmp_gt_u32_e32 vcc, s4, v7
	v_add_u32_e32 v10, 0x200, v7
	s_nop 0
	v_cndmask_b32_e32 v9, v5, v3, vcc
	v_cndmask_b32_e32 v8, v4, v2, vcc
	global_load_dword v209, v[8:9], off
	v_mov_b32_e32 v7, v10
	v_lshl_add_u64 v[4:5], v[4:5], 0, s[36:37]
	v_lshl_add_u64 v[2:3], v[2:3], 0, s[36:37]
	v_cmp_gt_u32_e32 vcc, s4, v7
	v_add_u32_e32 v10, 0x200, v7
	s_nop 0
	v_cndmask_b32_e32 v9, v5, v3, vcc
	v_cndmask_b32_e32 v8, v4, v2, vcc
	global_load_dword v210, v[8:9], off
	v_mov_b32_e32 v7, v10
	v_lshl_add_u64 v[4:5], v[4:5], 0, s[36:37]
	v_lshl_add_u64 v[2:3], v[2:3], 0, s[36:37]
	v_cmp_gt_u32_e32 vcc, s4, v7
	v_add_u32_e32 v10, 0x200, v7
	s_nop 0
	v_cndmask_b32_e32 v9, v5, v3, vcc
	v_cndmask_b32_e32 v8, v4, v2, vcc
	global_load_dword v211, v[8:9], off
	v_mov_b32_e32 v7, v10
	v_lshl_add_u64 v[4:5], v[4:5], 0, s[36:37]
	v_lshl_add_u64 v[2:3], v[2:3], 0, s[36:37]
	s_waitcnt vmcnt(11)
	v_mul_f32_e32 v9, 0xbfb8aa3b, v200
	v_exp_f32_e32 v9, v9
	s_nop 0
	v_add_f32_e32 v9, 1.0, v9
	v_div_scale_f32 v10, s[4:5], v9, v9, v200
	v_rcp_f32_e32 v11, v10
	v_div_scale_f32 v12, vcc, v200, v9, v200
	v_fma_f32 v13, -v10, v11, 1.0
	v_fmac_f32_e32 v11, v13, v11
	v_mul_f32_e32 v13, v12, v11
	v_fma_f32 v16, -v10, v13, v12
	v_fmac_f32_e32 v13, v16, v11
	v_fma_f32 v10, -v10, v13, v12
	v_div_fmas_f32 v10, v10, v11, v13
	v_div_fixup_f32 v8, v10, v9, v200
	ds_write_b32 v6, v8
	v_add_u32_e32 v6, 0x800, v6
	s_waitcnt vmcnt(10)
	v_mul_f32_e32 v9, 0xbfb8aa3b, v201
	v_exp_f32_e32 v9, v9
	s_nop 0
	v_add_f32_e32 v9, 1.0, v9
	v_div_scale_f32 v10, s[4:5], v9, v9, v201
	v_rcp_f32_e32 v11, v10
	v_div_scale_f32 v12, vcc, v201, v9, v201
	v_fma_f32 v13, -v10, v11, 1.0
	v_fmac_f32_e32 v11, v13, v11
	v_mul_f32_e32 v13, v12, v11
	v_fma_f32 v16, -v10, v13, v12
	v_fmac_f32_e32 v13, v16, v11
	v_fma_f32 v10, -v10, v13, v12
	v_div_fmas_f32 v10, v10, v11, v13
	v_div_fixup_f32 v8, v10, v9, v201
	ds_write_b32 v6, v8
	v_add_u32_e32 v6, 0x800, v6
	s_waitcnt vmcnt(9)
	v_mul_f32_e32 v9, 0xbfb8aa3b, v202
	v_exp_f32_e32 v9, v9
	s_nop 0
	v_add_f32_e32 v9, 1.0, v9
	v_div_scale_f32 v10, s[4:5], v9, v9, v202
	v_rcp_f32_e32 v11, v10
	v_div_scale_f32 v12, vcc, v202, v9, v202
	v_fma_f32 v13, -v10, v11, 1.0
	v_fmac_f32_e32 v11, v13, v11
	v_mul_f32_e32 v13, v12, v11
	v_fma_f32 v16, -v10, v13, v12
	v_fmac_f32_e32 v13, v16, v11
	v_fma_f32 v10, -v10, v13, v12
	v_div_fmas_f32 v10, v10, v11, v13
	v_div_fixup_f32 v8, v10, v9, v202
	ds_write_b32 v6, v8
	v_add_u32_e32 v6, 0x800, v6
	s_waitcnt vmcnt(8)
	v_mul_f32_e32 v9, 0xbfb8aa3b, v203
	v_exp_f32_e32 v9, v9
	s_nop 0
	v_add_f32_e32 v9, 1.0, v9
	v_div_scale_f32 v10, s[4:5], v9, v9, v203
	v_rcp_f32_e32 v11, v10
	v_div_scale_f32 v12, vcc, v203, v9, v203
	v_fma_f32 v13, -v10, v11, 1.0
	v_fmac_f32_e32 v11, v13, v11
	v_mul_f32_e32 v13, v12, v11
	v_fma_f32 v16, -v10, v13, v12
	v_fmac_f32_e32 v13, v16, v11
	v_fma_f32 v10, -v10, v13, v12
	v_div_fmas_f32 v10, v10, v11, v13
	v_div_fixup_f32 v8, v10, v9, v203
	ds_write_b32 v6, v8
	v_add_u32_e32 v6, 0x800, v6
	s_waitcnt vmcnt(7)
; __device__ __forceinline__ float silu_f(float x) { return x / (1.0f + __expf(-x)); }
; __device__ __forceinline__ void adaln_item(Frame& F, const float* wmod, const float* bmod, float* mod, int slab) {
;     ...
;     for (int i = F.tid; i < 3 * DM; i += NWAVES * 64) { const float x = i < 2 * DM ? c[i] : cc[i - 2 * DM]; sl[i] = silu_f(x); }
;     __syncthreads();
;     f32x4 a0 = {0.f, 0.f, 0.f, 0.f}, a1 = a0, a2 = a0;
; __device__ __forceinline__ void p0_prologue(Frame& F) {
;     for (int it = F.vcu; it < 192; it += F.G) { const int layer = it / 96, slab = it % 96;
;         adaln_item(F, F.in[layer ? 16 : 4], F.in[layer ? 17 : 5], WSP(float, layer ? WS_MOD1 : WS_MOD0), slab); }
	v_mul_f32_e32 v9, 0xbfb8aa3b, v204
	v_exp_f32_e32 v9, v9
	s_nop 0
	v_add_f32_e32 v9, 1.0, v9
	v_div_scale_f32 v10, s[4:5], v9, v9, v204
	v_rcp_f32_e32 v11, v10
	v_div_scale_f32 v12, vcc, v204, v9, v204
	v_fma_f32 v13, -v10, v11, 1.0
	v_fmac_f32_e32 v11, v13, v11
	v_mul_f32_e32 v13, v12, v11
	v_fma_f32 v16, -v10, v13, v12
	v_fmac_f32_e32 v13, v16, v11
	v_fma_f32 v10, -v10, v13, v12
	v_div_fmas_f32 v10, v10, v11, v13
	v_div_fixup_f32 v8, v10, v9, v204
	ds_write_b32 v6, v8
	v_add_u32_e32 v6, 0x800, v6
	s_waitcnt vmcnt(6)
	v_mul_f32_e32 v9, 0xbfb8aa3b, v205
	v_exp_f32_e32 v9, v9
	s_nop 0
	v_add_f32_e32 v9, 1.0, v9
	v_div_scale_f32 v10, s[4:5], v9, v9, v205
	v_rcp_f32_e32 v11, v10
	v_div_scale_f32 v12, vcc, v205, v9, v205
	v_fma_f32 v13, -v10, v11, 1.0
	v_fmac_f32_e32 v11, v13, v11
	v_mul_f32_e32 v13, v12, v11
	v_fma_f32 v16, -v10, v13, v12
	v_fmac_f32_e32 v13, v16, v11
	v_fma_f32 v10, -v10, v13, v12
	v_div_fmas_f32 v10, v10, v11, v13
	v_div_fixup_f32 v8, v10, v9, v205
	ds_write_b32 v6, v8
	v_add_u32_e32 v6, 0x800, v6
	s_waitcnt vmcnt(5)
	v_mul_f32_e32 v9, 0xbfb8aa3b, v206
	v_exp_f32_e32 v9, v9
	s_nop 0
	v_add_f32_e32 v9, 1.0, v9
	v_div_scale_f32 v10, s[4:5], v9, v9, v206
	v_rcp_f32_e32 v11, v10
	v_div_scale_f32 v12, vcc, v206, v9, v206
	v_fma_f32 v13, -v10, v11, 1.0
	v_fmac_f32_e32 v11, v13, v11
	v_mul_f32_e32 v13, v12, v11
	v_fma_f32 v16, -v10, v13, v12
	v_fmac_f32_e32 v13, v16, v11
	v_fma_f32 v10, -v10, v13, v12
	v_div_fmas_f32 v10, v10, v11, v13
	v_div_fixup_f32 v8, v10, v9, v206
	ds_write_b32 v6, v8
	v_add_u32_e32 v6, 0x800, v6
	s_waitcnt vmcnt(4)
	v_mul_f32_e32 v9, 0xbfb8aa3b, v207
	v_exp_f32_e32 v9, v9
	s_nop 0
	v_add_f32_e32 v9, 1.0, v9
	v_div_scale_f32 v10, s[4:5], v9, v9, v207
	v_rcp_f32_e32 v11, v10
	v_div_scale_f32 v12, vcc, v207, v9, v207
	v_fma_f32 v13, -v10, v11, 1.0
	v_fmac_f32_e32 v11, v13, v11
	v_mul_f32_e32 v13, v12, v11
	v_fma_f32 v16, -v10, v13, v12
	v_fmac_f32_e32 v13, v16, v11
	v_fma_f32 v10, -v10, v13, v12
	v_div_fmas_f32 v10, v10, v11, v13
	v_div_fixup_f32 v8, v10, v9, v207
	ds_write_b32 v6, v8
	v_add_u32_e32 v6, 0x800, v6
	s_waitcnt vmcnt(3)
	v_mul_f32_e32 v9, 0xbfb8aa3b, v208
	v_exp_f32_e32 v9, v9
	s_nop 0
	v_add_f32_e32 v9, 1.0, v9
	v_div_scale_f32 v10, s[4:5], v9, v9, v208
	v_rcp_f32_e32 v11, v10
	v_div_scale_f32 v12, vcc, v208, v9, v208
	v_fma_f32 v13, -v10, v11, 1.0
	v_fmac_f32_e32 v11, v13, v11
	v_mul_f32_e32 v13, v12, v11
	v_fma_f32 v16, -v10, v13, v12
	v_fmac_f32_e32 v13, v16, v11
	v_fma_f32 v10, -v10, v13, v12
	v_div_fmas_f32 v10, v10, v11, v13
	v_div_fixup_f32 v8, v10, v9, v208
	ds_write_b32 v6, v8
	v_add_u32_e32 v6, 0x800, v6
	s_waitcnt vmcnt(2)
	v_mul_f32_e32 v9, 0xbfb8aa3b, v209
	v_exp_f32_e32 v9, v9
	s_nop 0
	v_add_f32_e32 v9, 1.0, v9
	v_div_scale_f32 v10, s[4:5], v9, v9, v209
	v_rcp_f32_e32 v11, v10
	v_div_scale_f32 v12, vcc, v209, v9, v209
	v_fma_f32 v13, -v10, v11, 1.0
	v_fmac_f32_e32 v11, v13, v11
	v_mul_f32_e32 v13, v12, v11
	v_fma_f32 v16, -v10, v13, v12
	v_fmac_f32_e32 v13, v16, v11
	v_fma_f32 v10, -v10, v13, v12
	v_div_fmas_f32 v10, v10, v11, v13
	v_div_fixup_f32 v8, v10, v9, v209
	ds_write_b32 v6, v8
	v_add_u32_e32 v6, 0x800, v6
	s_waitcnt vmcnt(1)
	v_mul_f32_e32 v9, 0xbfb8aa3b, v210
	v_exp_f32_e32 v9, v9
	s_nop 0
	v_add_f32_e32 v9, 1.0, v9
	v_div_scale_f32 v10, s[4:5], v9, v9, v210
	v_rcp_f32_e32 v11, v10
	v_div_scale_f32 v12, vcc, v210, v9, v210
	v_fma_f32 v13, -v10, v11, 1.0
	v_fmac_f32_e32 v11, v13, v11
	v_mul_f32_e32 v13, v12, v11
	v_fma_f32 v16, -v10, v13, v12
	v_fmac_f32_e32 v13, v16, v11
	v_fma_f32 v10, -v10, v13, v12
	v_div_fmas_f32 v10, v10, v11, v13
	v_div_fixup_f32 v8, v10, v9, v210
	ds_write_b32 v6, v8
	v_add_u32_e32 v6, 0x800, v6
	s_waitcnt vmcnt(0)
	v_mul_f32_e32 v9, 0xbfb8aa3b, v211
	v_exp_f32_e32 v9, v9
	s_nop 0
	v_add_f32_e32 v9, 1.0, v9
	v_div_scale_f32 v10, s[4:5], v9, v9, v211
	v_rcp_f32_e32 v11, v10
	v_div_scale_f32 v12, vcc, v211, v9, v211
	v_fma_f32 v13, -v10, v11, 1.0
	v_fmac_f32_e32 v11, v13, v11
	v_mul_f32_e32 v13, v12, v11
	v_fma_f32 v16, -v10, v13, v12
	v_fmac_f32_e32 v13, v16, v11
	v_fma_f32 v10, -v10, v13, v12
	v_div_fmas_f32 v10, v10, v11, v13
	v_div_fixup_f32 v8, v10, v9, v211
	ds_write_b32 v6, v8
	v_add_u32_e32 v6, 0x800, v6
	s_or_b64 exec, exec, s[2:3]
	s_mul_hi_i32 s2, s33, 0x2aaaaaab
	s_lshr_b32 s3, s2, 31
	s_lshr_b32 s2, s2, 4
	s_add_i32 s2, s2, s3
	s_mulk_i32 s2, 0x60
	s_sub_i32 s2, s33, s2
	s_add_i32 s3, s33, 0x5f
	s_cmpk_lt_u32 s3, 0xbf
	s_cselect_b64 s[40:41], -1, 0
	s_lshl_b32 s38, s2, 7
	v_readlane_b32 s4, v250, 8
	v_readlane_b32 s44, v250, 63
	s_and_b64 s[2:3], s[40:41], exec
	v_readlane_b32 s12, v250, 16
	v_readlane_b32 s13, v250, 17
	v_readlane_b32 s45, v249, 0
	s_cselect_b32 s3, s13, s45
	s_cselect_b32 s2, s12, s44
	v_or_b32_e32 v2, s38, v1
	v_ashrrev_i32_e32 v3, 31, v2
	v_lshl_add_u64 v[4:5], s[2:3], 0, v[24:25]
	v_mov_b32_e32 v6, 0
	v_lshl_add_u64 v[26:27], v[2:3], 2, v[4:5]
	s_mov_b64 s[42:43], 0
	v_mov_b32_e32 v16, v53
	v_mov_b32_e32 v7, v6
	v_mov_b32_e32 v8, v6
	v_mov_b32_e32 v9, v6
	v_mov_b32_e32 v10, v6
	v_mov_b32_e32 v11, v6
	v_mov_b32_e32 v12, v6
	v_mov_b32_e32 v13, v6
	v_mov_b32_e32 v2, v6
	v_mov_b32_e32 v3, v6
	v_mov_b32_e32 v4, v6
	v_mov_b32_e32 v5, v6
	v_readlane_b32 s5, v250, 9
	v_readlane_b32 s6, v250, 10
	v_readlane_b32 s7, v250, 11
	v_readlane_b32 s8, v250, 12
	v_readlane_b32 s9, v250, 13
	v_readlane_b32 s10, v250, 14
	v_readlane_b32 s11, v250, 15
	v_readlane_b32 s14, v250, 18
	v_readlane_b32 s15, v250, 19
	v_readlane_b32 s16, v250, 20
	v_readlane_b32 s17, v250, 21
	v_readlane_b32 s18, v250, 22
	v_readlane_b32 s19, v250, 23
	v_readlane_b32 s46, v249, 1
	v_readlane_b32 s47, v249, 2
	v_readlane_b32 s48, v249, 3
	v_readlane_b32 s49, v249, 4
	v_readlane_b32 s50, v249, 5
	v_readlane_b32 s51, v249, 6
	v_readlane_b32 s52, v249, 7
	v_readlane_b32 s53, v249, 8
	v_readlane_b32 s54, v249, 9
	v_readlane_b32 s55, v249, 10
	v_readlane_b32 s56, v249, 11
	v_readlane_b32 s57, v249, 12
	v_readlane_b32 s58, v249, 13
	v_readlane_b32 s59, v249, 14
	s_waitcnt lgkmcnt(0)
	s_barrier

; #define GAS __attribute__((address_space(1)))
; __device__ __forceinline__ void route_phase(Frame& F) {
;     ...
;         __syncthreads();
;         if (F.tid < 8) lcnt[F.tid] = 0;
;         __syncthreads();
;         for (int i = 0; i < 8; ++i) { const int row = base + F.wave * 8 + i;
;             const float* mv = mod + (size_t)(row >> 13) * MOD_W;
;     ...
;             for (int j = 0; j < 8; ++j) { const int col = 4 * (F.lane + 64 * j);
;                 const f32x4 gg = *(const GAS f32x4*)(g + col), sh = *(const GAS f32x4*)(mv + 3 * DM + col), sc = *(const GAS f32x4*)(mv + 4 * DM + col);
.LBB0_1742:
	s_barrier
	s_and_saveexec_b64 s[0:1], s[2:3]
	ds_write_b32 v128, v21
	s_or_b64 exec, exec, s[0:1]
	s_add_i32 s26, s42, s43
	s_ashr_i32 s0, s26, 13
	s_mul_hi_i32 s1, s0, 0xc000
	s_mul_i32 s0, s0, 0xc000
	s_add_u32 s8, s36, s0
	s_addc_u32 s9, s37, s1
	s_add_u32 s0, s8, 0x6000
	s_addc_u32 s1, s9, 0
	s_add_u32 s8, s8, 0x8000
	s_addc_u32 s9, s9, 0
	v_mov_b32_e32 v45, v21
	v_mov_b32_e32 v47, v21
	v_mov_b32_e32 v49, v21
	v_mov_b32_e32 v51, v21
	v_mov_b32_e32 v53, v21
	v_lshl_add_u64 v[54:55], s[0:1], 0, v[40:41]
	v_lshl_add_u64 v[56:57], s[8:9], 0, v[40:41]
	v_lshl_add_u64 v[58:59], s[0:1], 0, v[42:43]
	v_lshl_add_u64 v[60:61], s[8:9], 0, v[42:43]
	v_lshl_add_u64 v[62:63], s[0:1], 0, v[20:21]
	v_lshl_add_u64 v[64:65], s[8:9], 0, v[20:21]
	v_lshl_add_u64 v[66:67], s[0:1], 0, v[44:45]
	v_lshl_add_u64 v[68:69], s[8:9], 0, v[44:45]
	v_lshl_add_u64 v[70:71], s[0:1], 0, v[46:47]
	v_lshl_add_u64 v[72:73], s[8:9], 0, v[46:47]
	v_lshl_add_u64 v[74:75], s[0:1], 0, v[48:49]
	v_lshl_add_u64 v[76:77], s[8:9], 0, v[48:49]
	v_lshl_add_u64 v[78:79], s[0:1], 0, v[50:51]
	v_lshl_add_u64 v[80:81], s[8:9], 0, v[50:51]
	v_lshl_add_u64 v[82:83], s[0:1], 0, v[52:53]
	v_lshl_add_u64 v[84:85], s[8:9], 0, v[52:53]
	global_load_dwordx4 v[150:153], v[22:23], off
	global_load_dwordx4 v[154:157], v[54:55], off
	global_load_dwordx4 v[158:161], v[56:57], off
	global_load_dwordx4 v[162:165], v[22:23], off offset:1024
	global_load_dwordx4 v[166:169], v[58:59], off
	global_load_dwordx4 v[170:173], v[60:61], off
	global_load_dwordx4 v[174:177], v[22:23], off offset:2048
	global_load_dwordx4 v[182:185], v[62:63], off
	global_load_dwordx4 v[186:189], v[64:65], off
	global_load_dwordx4 v[190:193], v[22:23], off offset:3072
	global_load_dwordx4 v[194:197], v[66:67], off
	global_load_dwordx4 v[200:203], v[68:69], off
	global_load_dwordx4 v[204:207], v[24:25], off
	global_load_dwordx4 v[208:211], v[70:71], off
	global_load_dwordx4 v[212:215], v[72:73], off
	global_load_dwordx4 v[216:219], v[26:27], off
	global_load_dwordx4 v[220:223], v[74:75], off
	global_load_dwordx4 v[224:227], v[76:77], off
	global_load_dwordx4 v[228:231], v[28:29], off
	global_load_dwordx4 v[232:235], v[78:79], off
	global_load_dwordx4 v[236:239], v[80:81], off
	global_load_dwordx4 v[240:243], v[30:31], off
	global_load_dwordx4 v[244:247], v[82:83], off
	global_load_dwordx4 v[252:255], v[84:85], off
	s_mov_b32 s27, 0
	s_mov_b32 s28, s49
	s_mov_b32 s30, s47
	s_waitcnt lgkmcnt(0)
	s_barrier
	s_branch .LBB0_1746

; #define GAS __attribute__((address_space(1)))
; __device__ __forceinline__ void route_phase(Frame& F) {
;     ...
;         for (int i = 0; i < 8; ++i) { const int row = base + F.wave * 8 + i;
;             const float* mv = mod + (size_t)(row >> 13) * MOD_W;
;             const GAS v2u* xr = (const GAS v2u*)(WSP(const bf16, WS_H) + (size_t)row * DM) + F.lane;
;             f32x4 v[8]; float s = 0.f;
; #pragma unroll
;             for (int j = 0; j < 8; ++j) { const v2u w = xr[64 * j]; v[j].x = bflo(w.x); v[j].y = bfhi(w.x); v[j].z = bflo(w.y); v[j].w = bfhi(w.y); s += (v[j].x * v[j].x + v[j].y * v[j].y) + (v[j].z * v[j].z + v[j].w * v[j].w); }
;             const float rstd = 1.0f / sqrtf(wave_sum(s) * (1.0f / DM) + NORM_EPS);
.LBB0_1746:
	s_ashr_i32 s29, s28, 31
	s_lshl_b64 s[0:1], s[28:29], 12
	s_waitcnt lgkmcnt(5)
	v_lshl_add_u64 v[6:7], v[36:37], 0, s[0:1]
	global_load_dwordx2 v[4:5], v[6:7], off
	s_waitcnt lgkmcnt(3)
	global_load_dwordx2 v[10:11], v[6:7], off offset:512
	s_waitcnt lgkmcnt(1)
	global_load_dwordx2 v[14:15], v[6:7], off offset:1024
	global_load_dwordx2 v[18:19], v[6:7], off offset:1536
	s_lshl_b64 s[8:9], s[28:29], 11
	global_load_dwordx2 v[88:89], v[6:7], off offset:3072
	s_waitcnt vmcnt(4)
	v_lshlrev_b32_e32 v2, 16, v4
	v_and_b32_e32 v3, 0xffff0000, v4
	v_lshlrev_b32_e32 v4, 16, v5
	v_and_b32_e32 v5, 0xffff0000, v5
	v_mul_f32_e32 v8, v5, v5
	s_waitcnt vmcnt(3)
	v_and_b32_e32 v111, 0xffff0000, v11
	v_and_b32_e32 v110, 0xffff0000, v10
	s_waitcnt vmcnt(1)
	v_lshlrev_b32_e32 v107, 16, v18
	v_and_b32_e32 v105, 0xffff0000, v18
	v_mul_f32_e32 v18, v3, v3
	v_pk_fma_f32 v[8:9], v[4:5], v[4:5], v[8:9] op_sel_hi:[1,1,0]
	s_waitcnt lgkmcnt(0)
	v_lshlrev_b32_e32 v17, 16, v11
	v_lshlrev_b32_e32 v16, 16, v10
	v_pk_mul_f32 v[10:11], v[110:111], v[110:111]
	v_lshlrev_b32_e32 v108, 16, v19
	v_and_b32_e32 v109, 0xffff0000, v19
	v_pk_fma_f32 v[18:19], v[2:3], v[2:3], v[18:19] op_sel_hi:[1,1,0]
	v_pk_fma_f32 v[10:11], v[16:17], v[16:17], v[10:11]
	v_mov_b32_e32 v106, v18
	v_mov_b32_e32 v86, v8
	v_mov_b32_e32 v87, v107
	v_mul_f32_e32 v45, v105, v105
	v_pk_add_f32 v[8:9], v[18:19], v[8:9]
	v_pk_mul_f32 v[18:19], v[106:107], v[86:87]
	v_pk_add_f32 v[10:11], v[10:11], v[10:11] op_sel:[0,1] op_sel_hi:[1,0]
	v_lshlrev_b32_e32 v12, 16, v14
	v_and_b32_e32 v13, 0xffff0000, v14
	v_lshlrev_b32_e32 v14, 16, v15
	v_and_b32_e32 v15, 0xffff0000, v15
	v_mov_b32_e32 v9, v19
	v_mov_b32_e32 v11, v45
	v_pk_add_f32 v[8:9], v[8:9], v[10:11]
	v_mul_f32_e32 v10, v13, v13
	v_mul_f32_e32 v18, v15, v15
	v_mul_f32_e32 v47, v108, v108
	v_mul_f32_e32 v49, v109, v109
	v_pk_fma_f32 v[10:11], v[12:13], v[12:13], v[10:11] op_sel_hi:[1,1,0]
	v_pk_fma_f32 v[18:19], v[14:15], v[14:15], v[18:19] op_sel_hi:[1,1,0]
	v_mov_b32_e32 v11, v47
	v_mov_b32_e32 v19, v49
	v_pk_add_f32 v[10:11], v[10:11], v[18:19]
	global_load_dwordx2 v[86:87], v[6:7], off offset:2560
	v_pk_add_f32 v[8:9], v[8:9], v[10:11]
	global_load_dwordx2 v[10:11], v[6:7], off offset:2048
	v_mov_b32_e32 v104, v107
	global_load_dwordx2 v[6:7], v[6:7], off offset:3584
	s_waitcnt vmcnt(3)
	v_lshlrev_b32_e32 v96, 16, v89
	v_and_b32_e32 v97, 0xffff0000, v89
	v_and_b32_e32 v95, 0xffff0000, v88
	v_lshlrev_b32_e32 v94, 16, v88
	v_mov_b32_e32 v88, 0
	s_waitcnt vmcnt(2)
	v_and_b32_e32 v99, 0xffff0000, v87
	v_and_b32_e32 v98, 0xffff0000, v86
	s_waitcnt vmcnt(1)
	v_and_b32_e32 v103, 0xffff0000, v11
	v_and_b32_e32 v102, 0xffff0000, v10
	v_lshlrev_b32_e32 v101, 16, v11
	v_lshlrev_b32_e32 v100, 16, v10
	v_pk_mul_f32 v[10:11], v[102:103], v[102:103]
	s_waitcnt vmcnt(0)
	v_lshlrev_b32_e32 v91, 16, v6
	v_pk_fma_f32 v[10:11], v[100:101], v[100:101], v[10:11]
	v_and_b32_e32 v89, 0xffff0000, v6
	v_pk_add_f32 v[10:11], v[10:11], v[10:11] op_sel:[0,1] op_sel_hi:[1,0]
	v_lshlrev_b32_e32 v92, 16, v7
	v_and_b32_e32 v93, 0xffff0000, v7
	v_pk_add_f32 v[6:7], v[8:9], v[8:9] op_sel:[0,1] op_sel_hi:[1,0]
	v_lshlrev_b32_e32 v19, 16, v87
	v_lshlrev_b32_e32 v18, 16, v86
	v_pk_mul_f32 v[86:87], v[98:99], v[98:99]
	v_mov_b32_e32 v90, v6
	v_mov_b32_e32 v8, v10
	v_mov_b32_e32 v9, v91
	v_pk_fma_f32 v[86:87], v[18:19], v[18:19], v[86:87]
	v_pk_add_f32 v[6:7], v[6:7], v[10:11]
	v_pk_mul_f32 v[8:9], v[90:91], v[8:9]
	v_mul_f32_e32 v45, v89, v89
	v_mov_b32_e32 v7, v9
	v_pk_add_f32 v[8:9], v[86:87], v[86:87] op_sel:[0,1] op_sel_hi:[1,0]
	v_mul_f32_e32 v10, v97, v97
	v_mov_b32_e32 v9, v45
	v_pk_add_f32 v[6:7], v[6:7], v[8:9]
	v_mul_f32_e32 v8, v95, v95
	v_mul_f32_e32 v47, v92, v92
	v_mul_f32_e32 v49, v93, v93
	v_pk_fma_f32 v[8:9], v[94:95], v[94:95], v[8:9] op_sel_hi:[1,1,0]
	v_pk_fma_f32 v[10:11], v[96:97], v[96:97], v[10:11] op_sel_hi:[1,1,0]
	v_mov_b32_e32 v9, v47
	v_mov_b32_e32 v11, v49
	v_pk_add_f32 v[8:9], v[8:9], v[10:11]
	v_lshl_add_u64 v[86:87], v[38:39], 0, s[8:9]
	v_pk_add_f32 v[6:7], v[6:7], v[8:9]
	s_nop 0
	v_add_f32_e32 v6, v6, v7
	ds_bpermute_b32 v7, v1, v6
	s_waitcnt lgkmcnt(0)
	v_add_f32_e32 v6, v6, v7
	ds_bpermute_b32 v7, v120, v6
	s_waitcnt lgkmcnt(0)
	v_add_f32_e32 v6, v6, v7
	ds_bpermute_b32 v7, v121, v6
	s_waitcnt lgkmcnt(0)
	v_add_f32_e32 v6, v6, v7
	ds_bpermute_b32 v7, v122, v6
	s_waitcnt lgkmcnt(0)
	v_add_f32_e32 v6, v6, v7
	ds_bpermute_b32 v7, v123, v6
	s_waitcnt lgkmcnt(0)
	v_add_f32_e32 v6, v6, v7
	ds_bpermute_b32 v7, v124, v6
	s_waitcnt lgkmcnt(0)
; #define GAS __attribute__((address_space(1)))
; __device__ __forceinline__ unsigned pk4_fp8(float a, float b, float c, float d) { int p = 0; p = __builtin_amdgcn_cvt_pk_fp8_f32(a, b, p, false); p = __builtin_amdgcn_cvt_pk_fp8_f32(c, d, p, true); return (unsigned)p; }
; __device__ __forceinline__ float clamp8(float x) { return __builtin_fminf(__builtin_fmaxf(x, -448.0f), 448.0f); }
; __device__ __forceinline__ void route_phase(Frame& F) {
;     ...
;             const float rstd = 1.0f / sqrtf(wave_sum(s) * (1.0f / DM) + NORM_EPS);
;             GAS unsigned* o4 = (GAS unsigned*)((unsigned char*)XN + (size_t)row * DM) + F.lane;
;             float lg[8];
; #pragma unroll
;             for (int e = 0; e < 8; ++e) lg[e] = 0.f;
; #pragma unroll
;             for (int j = 0; j < 8; ++j) { const int col = 4 * (F.lane + 64 * j);
;                 const f32x4 gg = *(const GAS f32x4*)(g + col), sh = *(const GAS f32x4*)(mv + 3 * DM + col), sc = *(const GAS f32x4*)(mv + 4 * DM + col);
;                 const f32x4 y = v[j] * rstd * gg * (sc + 1.0f) + sh; o4[64 * j] = pk4_fp8(clamp8(y.x), clamp8(y.y), clamp8(y.z), clamp8(y.w));
; #pragma unroll
;                 for (int q = 0; q < 4; ++q) { const f32x4 w0 = rwl[((j * 4 + q) * 2 + 0) * 64 + F.lane], w1 = rwl[((j * 4 + q) * 2 + 1) * 64 + F.lane];
;                     lg[0] += y[q] * w0.x; lg[1] += y[q] * w0.y; lg[2] += y[q] * w0.z; lg[3] += y[q] * w0.w; lg[4] += y[q] * w1.x; lg[5] += y[q] * w1.y; lg[6] += y[q] * w1.z; lg[7] += y[q] * w1.w; } }
	v_add_f32_e32 v6, v6, v7
	v_fmamk_f32 v6, v6, 0x3a000000, v129
	v_cmp_gt_f32_e32 vcc, s50, v6
	v_mul_f32_e32 v7, 0x4f800000, v6
	s_nop 0
	v_cndmask_b32_e32 v6, v6, v7, vcc
	v_sqrt_f32_e32 v7, v6
	s_nop 0
	v_add_u32_e32 v8, -1, v7
	v_fma_f32 v9, -v8, v7, v6
	v_cmp_ge_f32_e64 s[0:1], 0, v9
	v_add_u32_e32 v9, 1, v7
	s_nop 0
	v_cndmask_b32_e64 v8, v7, v8, s[0:1]
	v_fma_f32 v7, -v9, v7, v6
	v_cmp_lt_f32_e64 s[0:1], 0, v7
	s_nop 1
	v_cndmask_b32_e64 v7, v8, v9, s[0:1]
	v_mul_f32_e32 v8, 0x37800000, v7
	v_cndmask_b32_e32 v7, v7, v8, vcc
	v_cmp_class_f32_e32 vcc, v6, v130
	s_nop 1
	v_cndmask_b32_e32 v6, v7, v6, vcc
	v_div_scale_f32 v7, s[0:1], v6, v6, 1.0
	v_rcp_f32_e32 v8, v7
	s_nop 0
	v_fma_f32 v9, -v7, v8, 1.0
	v_fmac_f32_e32 v8, v9, v8
	v_div_scale_f32 v9, vcc, 1.0, v6, 1.0
	v_mul_f32_e32 v10, v9, v8
	v_fma_f32 v11, -v7, v10, v9
	v_fmac_f32_e32 v10, v11, v8
	v_fma_f32 v7, -v7, v10, v9
	v_div_fmas_f32 v7, v7, v8, v10
	v_div_fixup_f32 v90, v7, v6, 1.0
	v_mov_b32_e32 v6, v150
	v_mov_b32_e32 v7, v151
	v_mov_b32_e32 v8, v152
	v_mov_b32_e32 v9, v153
	v_mov_b32_e32 v114, v154
	v_mov_b32_e32 v115, v155
	v_mov_b32_e32 v116, v156
	v_mov_b32_e32 v117, v157
	v_mov_b32_e32 v136, v158
	v_mov_b32_e32 v137, v159
	v_mov_b32_e32 v138, v160
	v_mov_b32_e32 v139, v161
	v_pk_mul_f32 v[4:5], v[90:91], v[4:5] op_sel_hi:[0,1]
	v_pk_mul_f32 v[2:3], v[90:91], v[2:3] op_sel_hi:[0,1]
	v_pk_mul_f32 v[14:15], v[90:91], v[14:15] op_sel_hi:[0,1]
	v_pk_mul_f32 v[12:13], v[90:91], v[12:13] op_sel_hi:[0,1]
	v_pk_mul_f32 v[104:105], v[104:105], v[90:91] op_sel_hi:[1,0]
	v_pk_mul_f32 v[94:95], v[90:91], v[94:95] op_sel_hi:[0,1]
	v_pk_mul_f32 v[92:93], v[92:93], v[90:91] op_sel_hi:[1,0]
	v_pk_mul_f32 v[2:3], v[6:7], v[2:3]
	v_pk_mul_f32 v[4:5], v[8:9], v[4:5]
	v_pk_add_f32 v[8:9], v[136:137], 1.0 op_sel_hi:[1,0]
	v_pk_add_f32 v[6:7], v[138:139], 1.0 op_sel_hi:[1,0]
	v_pk_fma_f32 v[114:115], v[8:9], v[2:3], v[114:115]
	v_pk_fma_f32 v[112:113], v[6:7], v[4:5], v[116:117]
	v_med3_f32 v2, v114, s51, v133
	v_med3_f32 v3, v115, s51, v133
	v_mov_b32_e32 v6, 0
	v_cvt_pk_fp8_f32 v6, v2, v3
	v_med3_f32 v4, v112, s51, v133
	v_med3_f32 v5, v113, s51, v133
	v_cvt_pk_fp8_f32 v6, v4, v5 op_sel:[0,0,1]
	global_store_dword v[86:87], v6, off
	ds_read_b128 v[2:5], v125 offset:2048
	ds_read_b128 v[6:9], v125 offset:3072
	s_waitcnt lgkmcnt(1)
	v_fma_f32 v136, v4, v114, 0
	v_fma_f32 v53, v5, v114, 0
	s_waitcnt lgkmcnt(0)
	v_fma_f32 v51, v6, v114, 0
	v_fma_f32 v49, v7, v114, 0
	v_fma_f32 v47, v8, v114, 0
	v_fma_f32 v45, v9, v114, 0
	ds_read_b128 v[4:7], v125 offset:4096
	ds_read_b128 v[8:11], v125 offset:5120
	v_pk_fma_f32 v[2:3], v[2:3], v[114:115], 0 op_sel_hi:[1,0,0]
	s_waitcnt lgkmcnt(1)
	v_fmac_f32_e32 v136, v6, v115
	v_fmac_f32_e32 v53, v7, v115
	s_waitcnt lgkmcnt(0)
	v_fmac_f32_e32 v51, v8, v115
	v_fmac_f32_e32 v49, v9, v115
	ds_read_b128 v[6:9], v125 offset:6144
	ds_read_b128 v[116:119], v125 offset:7168
	v_fmac_f32_e32 v47, v10, v115
	v_fmac_f32_e32 v45, v11, v115
	v_pk_fma_f32 v[2:3], v[4:5], v[114:115], v[2:3] op_sel:[0,1,0]
	s_waitcnt lgkmcnt(1)
	v_fmac_f32_e32 v136, v8, v112
	v_fmac_f32_e32 v53, v9, v112
	s_waitcnt lgkmcnt(0)
	v_fmac_f32_e32 v51, v116, v112
	v_fmac_f32_e32 v49, v117, v112
	v_fmac_f32_e32 v47, v118, v112
	v_fmac_f32_e32 v45, v119, v112
	ds_read_b128 v[8:11], v125 offset:8192
	ds_read_b128 v[116:119], v125 offset:9216
	v_pk_fma_f32 v[2:3], v[6:7], v[112:113], v[2:3] op_sel_hi:[1,0,1]
	s_waitcnt lgkmcnt(1)
	v_fmac_f32_e32 v136, v10, v113
	s_waitcnt lgkmcnt(0)
	v_fmac_f32_e32 v51, v116, v113
	v_fmac_f32_e32 v49, v117, v113
	v_fmac_f32_e32 v47, v118, v113
	v_fmac_f32_e32 v45, v119, v113
	v_mov_b32_e32 v116, v162
	v_mov_b32_e32 v117, v163
	v_mov_b32_e32 v118, v164
	v_mov_b32_e32 v119, v165
	v_mov_b32_e32 v138, v166
	v_mov_b32_e32 v139, v167
	v_mov_b32_e32 v140, v168
	v_mov_b32_e32 v141, v169
	v_mov_b32_e32 v142, v170
	v_mov_b32_e32 v143, v171
	v_mov_b32_e32 v144, v172
	v_mov_b32_e32 v145, v173
	v_mov_b32_e32 v10, v17
	v_mov_b32_e32 v17, v110
	v_fmac_f32_e32 v53, v11, v113
	v_mov_b32_e32 v11, v111
	v_pk_mul_f32 v[16:17], v[90:91], v[16:17] op_sel_hi:[0,1]
	v_pk_mul_f32 v[10:11], v[90:91], v[10:11] op_sel_hi:[0,1]
	v_pk_fma_f32 v[2:3], v[8:9], v[112:113], v[2:3] op_sel:[0,1,0]
	v_pk_mul_f32 v[16:17], v[16:17], v[116:117]
	v_pk_mul_f32 v[10:11], v[10:11], v[118:119]
	v_pk_add_f32 v[116:117], v[142:143], 1.0 op_sel_hi:[1,0]
	v_pk_add_f32 v[110:111], v[144:145], 1.0 op_sel_hi:[1,0]
	v_pk_fma_f32 v[116:117], v[16:17], v[116:117], v[138:139]
	v_pk_fma_f32 v[110:111], v[10:11], v[110:111], v[140:141]
	v_med3_f32 v10, v116, s51, v133
	v_med3_f32 v11, v117, s51, v133
	v_cvt_pk_fp8_f32 v88, v10, v11
	v_med3_f32 v16, v110, s51, v133
	v_med3_f32 v17, v111, s51, v133
	v_cvt_pk_fp8_f32 v88, v16, v17 op_sel:[0,0,1]
	global_store_dword v[86:87], v88, off offset:256
	ds_read_b128 v[138:141], v125 offset:10240
	ds_read_b128 v[142:145], v125 offset:11264
	s_waitcnt lgkmcnt(1)
	v_pk_fma_f32 v[112:113], v[116:117], v[138:139], v[2:3] op_sel_hi:[0,1,1]
	ds_read_b128 v[2:5], v125 offset:12288
	ds_read_b128 v[6:9], v125 offset:13312
	v_fmac_f32_e32 v136, v116, v140
	v_fmac_f32_e32 v53, v116, v141
	s_waitcnt lgkmcnt(2)
	v_fmac_f32_e32 v51, v116, v142
	v_fmac_f32_e32 v49, v116, v143
	v_fmac_f32_e32 v47, v116, v144
	v_fmac_f32_e32 v45, v116, v145
	s_waitcnt lgkmcnt(1)
	v_fmac_f32_e32 v136, v117, v4
	v_fmac_f32_e32 v53, v117, v5
	s_waitcnt lgkmcnt(0)
	v_fmac_f32_e32 v51, v117, v6
	v_fmac_f32_e32 v49, v117, v7
	v_fmac_f32_e32 v47, v117, v8
	v_fmac_f32_e32 v45, v117, v9
	ds_read_b128 v[4:7], v125 offset:14336
	ds_read_b128 v[8:11], v125 offset:15360
	v_pk_fma_f32 v[2:3], v[116:117], v[2:3], v[112:113] op_sel:[1,0,0]
	s_waitcnt lgkmcnt(1)
; #define GAS __attribute__((address_space(1)))
; __device__ __forceinline__ unsigned pk4_fp8(float a, float b, float c, float d) { int p = 0; p = __builtin_amdgcn_cvt_pk_fp8_f32(a, b, p, false); p = __builtin_amdgcn_cvt_pk_fp8_f32(c, d, p, true); return (unsigned)p; }
; __device__ __forceinline__ float clamp8(float x) { return __builtin_fminf(__builtin_fmaxf(x, -448.0f), 448.0f); }
; __device__ __forceinline__ void route_phase(Frame& F) {
;     ...
;             for (int j = 0; j < 8; ++j) { const int col = 4 * (F.lane + 64 * j);
;                 const f32x4 gg = *(const GAS f32x4*)(g + col), sh = *(const GAS f32x4*)(mv + 3 * DM + col), sc = *(const GAS f32x4*)(mv + 4 * DM + col);
;                 const f32x4 y = v[j] * rstd * gg * (sc + 1.0f) + sh; o4[64 * j] = pk4_fp8(clamp8(y.x), clamp8(y.y), clamp8(y.z), clamp8(y.w));
; #pragma unroll
;                 for (int q = 0; q < 4; ++q) { const f32x4 w0 = rwl[((j * 4 + q) * 2 + 0) * 64 + F.lane], w1 = rwl[((j * 4 + q) * 2 + 1) * 64 + F.lane];
;                     lg[0] += y[q] * w0.x; lg[1] += y[q] * w0.y; lg[2] += y[q] * w0.z; lg[3] += y[q] * w0.w; lg[4] += y[q] * w1.x; lg[5] += y[q] * w1.y; lg[6] += y[q] * w1.z; lg[7] += y[q] * w1.w; } }
	v_fmac_f32_e32 v136, v110, v6
	v_fmac_f32_e32 v53, v110, v7
	s_waitcnt lgkmcnt(0)
	v_fmac_f32_e32 v51, v110, v8
	v_fmac_f32_e32 v49, v110, v9
	ds_read_b128 v[6:9], v125 offset:16384
	ds_read_b128 v[138:141], v125 offset:17408
	v_fmac_f32_e32 v47, v110, v10
	v_fmac_f32_e32 v45, v110, v11
	v_pk_fma_f32 v[2:3], v[110:111], v[4:5], v[2:3] op_sel_hi:[0,1,1]
	s_waitcnt lgkmcnt(1)
	v_fmac_f32_e32 v136, v111, v8
	v_fmac_f32_e32 v53, v111, v9
	s_waitcnt lgkmcnt(0)
	v_fmac_f32_e32 v51, v111, v138
	v_fmac_f32_e32 v49, v111, v139
	v_fmac_f32_e32 v47, v111, v140
	v_fmac_f32_e32 v45, v111, v141
	v_mov_b32_e32 v8, v174
	v_mov_b32_e32 v9, v175
	v_mov_b32_e32 v10, v176
	v_mov_b32_e32 v11, v177
	v_mov_b32_e32 v138, v182
	v_mov_b32_e32 v139, v183
	v_mov_b32_e32 v140, v184
	v_mov_b32_e32 v141, v185
	v_mov_b32_e32 v142, v186
	v_mov_b32_e32 v143, v187
	v_mov_b32_e32 v144, v188
	v_mov_b32_e32 v145, v189
	v_pk_fma_f32 v[2:3], v[110:111], v[6:7], v[2:3] op_sel:[1,0,0]
	v_mov_b32_e32 v110, v19
	v_mov_b32_e32 v19, v98
	v_pk_mul_f32 v[18:19], v[90:91], v[18:19] op_sel_hi:[0,1]
	v_mov_b32_e32 v111, v99
	v_pk_mul_f32 v[110:111], v[90:91], v[110:111] op_sel_hi:[0,1]
	v_pk_mul_f32 v[8:9], v[12:13], v[8:9]
	v_pk_mul_f32 v[10:11], v[14:15], v[10:11]
	v_pk_add_f32 v[14:15], v[142:143], 1.0 op_sel_hi:[1,0]
	v_pk_add_f32 v[12:13], v[144:145], 1.0 op_sel_hi:[1,0]
	v_pk_fma_f32 v[118:119], v[8:9], v[14:15], v[138:139]
	v_pk_fma_f32 v[114:115], v[10:11], v[12:13], v[140:141]
	v_med3_f32 v8, v118, s51, v133
	v_med3_f32 v9, v119, s51, v133
	v_mov_b32_e32 v12, 0
	v_cvt_pk_fp8_f32 v12, v8, v9
	v_med3_f32 v10, v114, s51, v133
	v_med3_f32 v11, v115, s51, v133
	v_cvt_pk_fp8_f32 v12, v10, v11 op_sel:[0,0,1]
	global_store_dword v[86:87], v12, off offset:512
	ds_read_b128 v[8:11], v125 offset:18432
	ds_read_b128 v[12:15], v125 offset:19456
	s_waitcnt lgkmcnt(1)
	v_fmac_f32_e32 v136, v118, v10
	v_fmac_f32_e32 v53, v118, v11
	s_waitcnt lgkmcnt(0)
	v_fmac_f32_e32 v51, v118, v12
	v_fmac_f32_e32 v49, v118, v13
	v_fmac_f32_e32 v47, v118, v14
	v_fmac_f32_e32 v45, v118, v15
	ds_read_b128 v[10:13], v125 offset:20480
	ds_read_b128 v[14:17], v125 offset:21504
	v_pk_fma_f32 v[2:3], v[118:119], v[8:9], v[2:3] op_sel_hi:[0,1,1]
	s_waitcnt lgkmcnt(1)
	v_fmac_f32_e32 v136, v119, v12
	v_fmac_f32_e32 v53, v119, v13
	s_waitcnt lgkmcnt(0)
	v_fmac_f32_e32 v51, v119, v14
	v_fmac_f32_e32 v49, v119, v15
	ds_read_b128 v[12:15], v125 offset:22528
	ds_read_b128 v[138:141], v125 offset:23552
	v_fmac_f32_e32 v47, v119, v16
	v_fmac_f32_e32 v45, v119, v17
	v_pk_fma_f32 v[2:3], v[118:119], v[10:11], v[2:3] op_sel:[1,0,0]
	s_waitcnt lgkmcnt(1)
	v_fmac_f32_e32 v136, v114, v14
	v_fmac_f32_e32 v53, v114, v15
	s_waitcnt lgkmcnt(0)
	v_fmac_f32_e32 v51, v114, v138
	v_fmac_f32_e32 v49, v114, v139
	v_fmac_f32_e32 v47, v114, v140
	v_fmac_f32_e32 v45, v114, v141
	ds_read_b128 v[14:17], v125 offset:24576
	ds_read_b128 v[138:141], v125 offset:25600
	v_pk_fma_f32 v[2:3], v[114:115], v[12:13], v[2:3] op_sel_hi:[0,1,1]
	s_waitcnt lgkmcnt(1)
	v_fmac_f32_e32 v136, v115, v16
	s_waitcnt lgkmcnt(0)
	v_fmac_f32_e32 v51, v115, v138
	v_fmac_f32_e32 v49, v115, v139
	v_fmac_f32_e32 v47, v115, v140
	v_fmac_f32_e32 v45, v115, v141
	v_mov_b32_e32 v138, v190
	v_mov_b32_e32 v139, v191
	v_mov_b32_e32 v140, v192
	v_mov_b32_e32 v141, v193
	v_mov_b32_e32 v142, v194
	v_mov_b32_e32 v143, v195
	v_mov_b32_e32 v144, v196
	v_mov_b32_e32 v145, v197
	v_mov_b32_e32 v146, v200
	v_mov_b32_e32 v147, v201
	v_mov_b32_e32 v148, v202
	v_mov_b32_e32 v149, v203
	v_fmac_f32_e32 v53, v115, v17
	v_pk_mul_f32 v[16:17], v[108:109], v[90:91] op_sel_hi:[1,0]
	v_pk_fma_f32 v[2:3], v[114:115], v[14:15], v[2:3] op_sel:[1,0,0]
	v_mov_b32_e32 v14, v101
	v_mov_b32_e32 v101, v102
	v_mov_b32_e32 v15, v103
	v_pk_mul_f32 v[14:15], v[90:91], v[14:15] op_sel_hi:[0,1]
	v_pk_mul_f32 v[104:105], v[104:105], v[138:139]
	v_pk_mul_f32 v[16:17], v[16:17], v[140:141]
	v_pk_add_f32 v[108:109], v[146:147], 1.0 op_sel_hi:[1,0]
	v_pk_add_f32 v[106:107], v[148:149], 1.0 op_sel_hi:[1,0]
	v_pk_fma_f32 v[148:149], v[104:105], v[108:109], v[142:143]
	v_pk_fma_f32 v[16:17], v[16:17], v[106:107], v[144:145]
	v_med3_f32 v88, v148, s51, v133
	v_med3_f32 v104, v149, s51, v133
	v_mov_b32_e32 v107, 0
	v_cvt_pk_fp8_f32 v107, v88, v104
	v_med3_f32 v105, v16, s51, v133
	v_med3_f32 v106, v17, s51, v133
	v_cvt_pk_fp8_f32 v107, v105, v106 op_sel:[0,0,1]
	global_store_dword v[86:87], v107, off offset:768
	ds_read_b128 v[104:107], v125 offset:26624
	ds_read_b128 v[138:141], v125 offset:27648
	s_waitcnt lgkmcnt(1)
	v_fmac_f32_e32 v136, v148, v106
	v_fmac_f32_e32 v53, v148, v107
	s_waitcnt lgkmcnt(0)
	v_fmac_f32_e32 v51, v148, v138
	v_fmac_f32_e32 v49, v148, v139
	v_fmac_f32_e32 v47, v148, v140
	v_fmac_f32_e32 v45, v148, v141
	ds_read_b128 v[106:109], v125 offset:28672
	ds_read_b128 v[138:141], v125 offset:29696
	v_pk_fma_f32 v[2:3], v[148:149], v[104:105], v[2:3] op_sel_hi:[0,1,1]
	s_waitcnt lgkmcnt(1)
	v_fmac_f32_e32 v136, v149, v108
	s_waitcnt lgkmcnt(0)
	v_fmac_f32_e32 v51, v149, v138
	v_fmac_f32_e32 v49, v149, v139
	v_fmac_f32_e32 v47, v149, v140
	v_fmac_f32_e32 v45, v149, v141
	ds_read_b128 v[138:141], v125 offset:30720
	ds_read_b128 v[142:145], v125 offset:31744
	v_fmac_f32_e32 v53, v149, v109
	v_pk_fma_f32 v[2:3], v[148:149], v[106:107], v[2:3] op_sel:[1,0,0]
	s_waitcnt lgkmcnt(1)
	v_fmac_f32_e32 v136, v16, v140
	v_fmac_f32_e32 v53, v16, v141
	s_waitcnt lgkmcnt(0)
	v_fmac_f32_e32 v51, v16, v142
	v_fmac_f32_e32 v49, v16, v143
	v_fmac_f32_e32 v47, v16, v144
	v_fmac_f32_e32 v45, v16, v145
	ds_read_b128 v[140:143], v125 offset:32768
	ds_read_b128 v[144:147], v125 offset:33792
	v_pk_fma_f32 v[2:3], v[16:17], v[138:139], v[2:3] op_sel_hi:[0,1,1]
	s_waitcnt lgkmcnt(1)
; #define GAS __attribute__((address_space(1)))
; __device__ __forceinline__ unsigned pk4_fp8(float a, float b, float c, float d) { int p = 0; p = __builtin_amdgcn_cvt_pk_fp8_f32(a, b, p, false); p = __builtin_amdgcn_cvt_pk_fp8_f32(c, d, p, true); return (unsigned)p; }
; __device__ __forceinline__ float clamp8(float x) { return __builtin_fminf(__builtin_fmaxf(x, -448.0f), 448.0f); }
; __device__ __forceinline__ void route_phase(Frame& F) {
;     ...
;             for (int j = 0; j < 8; ++j) { const int col = 4 * (F.lane + 64 * j);
;                 const f32x4 gg = *(const GAS f32x4*)(g + col), sh = *(const GAS f32x4*)(mv + 3 * DM + col), sc = *(const GAS f32x4*)(mv + 4 * DM + col);
;                 const f32x4 y = v[j] * rstd * gg * (sc + 1.0f) + sh; o4[64 * j] = pk4_fp8(clamp8(y.x), clamp8(y.y), clamp8(y.z), clamp8(y.w));
; #pragma unroll
;                 for (int q = 0; q < 4; ++q) { const f32x4 w0 = rwl[((j * 4 + q) * 2 + 0) * 64 + F.lane], w1 = rwl[((j * 4 + q) * 2 + 1) * 64 + F.lane];
;                     lg[0] += y[q] * w0.x; lg[1] += y[q] * w0.y; lg[2] += y[q] * w0.z; lg[3] += y[q] * w0.w; lg[4] += y[q] * w1.x; lg[5] += y[q] * w1.y; lg[6] += y[q] * w1.z; lg[7] += y[q] * w1.w; } }
	v_pk_fma_f32 v[104:105], v[16:17], v[140:141], v[2:3] op_sel:[1,0,0]
	v_mov_b32_e32 v2, v204
	v_mov_b32_e32 v3, v205
	v_mov_b32_e32 v4, v206
	v_mov_b32_e32 v5, v207
	v_mov_b32_e32 v6, v208
	v_mov_b32_e32 v7, v209
	v_mov_b32_e32 v8, v210
	v_mov_b32_e32 v9, v211
	v_mov_b32_e32 v10, v212
	v_mov_b32_e32 v11, v213
	v_mov_b32_e32 v12, v214
	v_mov_b32_e32 v13, v215
	v_fmac_f32_e32 v136, v17, v142
	v_fmac_f32_e32 v53, v17, v143
	s_waitcnt lgkmcnt(0)
	v_fmac_f32_e32 v51, v17, v144
	v_fmac_f32_e32 v49, v17, v145
	v_fmac_f32_e32 v47, v17, v146
	v_fmac_f32_e32 v45, v17, v147
	v_pk_mul_f32 v[16:17], v[90:91], v[100:101] op_sel_hi:[0,1]
	v_pk_mul_f32 v[2:3], v[16:17], v[2:3]
	v_pk_mul_f32 v[4:5], v[14:15], v[4:5]
	v_pk_add_f32 v[10:11], v[10:11], 1.0 op_sel_hi:[1,0]
	v_pk_add_f32 v[12:13], v[12:13], 1.0 op_sel_hi:[1,0]
	v_pk_fma_f32 v[102:103], v[2:3], v[10:11], v[6:7]
	v_mov_b32_e32 v6, 0
	v_med3_f32 v2, v102, s51, v133
	v_med3_f32 v3, v103, s51, v133
	v_cvt_pk_fp8_f32 v6, v2, v3
	v_pk_fma_f32 v[100:101], v[4:5], v[12:13], v[8:9]
	s_nop 0
	v_med3_f32 v4, v100, s51, v133
	v_med3_f32 v5, v101, s51, v133
	v_cvt_pk_fp8_f32 v6, v4, v5 op_sel:[0,0,1]
	global_store_dword v[86:87], v6, off offset:1024
	ds_read_b128 v[2:5], v125 offset:34816
	ds_read_b128 v[6:9], v125 offset:35840
	s_waitcnt lgkmcnt(1)
	v_fmac_f32_e32 v136, v102, v4
	v_fmac_f32_e32 v53, v102, v5
	s_waitcnt lgkmcnt(0)
	v_fmac_f32_e32 v51, v102, v6
	v_fmac_f32_e32 v49, v102, v7
	v_fmac_f32_e32 v47, v102, v8
	v_fmac_f32_e32 v45, v102, v9
	ds_read_b128 v[4:7], v125 offset:36864
	ds_read_b128 v[8:11], v125 offset:37888
	v_pk_fma_f32 v[2:3], v[102:103], v[2:3], v[104:105] op_sel_hi:[0,1,1]
	s_waitcnt lgkmcnt(1)
	v_fmac_f32_e32 v136, v103, v6
	v_fmac_f32_e32 v53, v103, v7
	s_waitcnt lgkmcnt(0)
	v_fmac_f32_e32 v51, v103, v8
	v_fmac_f32_e32 v49, v103, v9
	v_fmac_f32_e32 v47, v103, v10
	v_fmac_f32_e32 v45, v103, v11
	ds_read_b128 v[6:9], v125 offset:38912
	ds_read_b128 v[10:13], v125 offset:39936
	v_pk_fma_f32 v[2:3], v[102:103], v[4:5], v[2:3] op_sel:[1,0,0]
	s_waitcnt lgkmcnt(1)
	v_fmac_f32_e32 v136, v100, v8
	v_fmac_f32_e32 v53, v100, v9
	s_waitcnt lgkmcnt(0)
	v_fmac_f32_e32 v51, v100, v10
	v_fmac_f32_e32 v49, v100, v11
	v_fmac_f32_e32 v47, v100, v12
	v_fmac_f32_e32 v45, v100, v13
	ds_read_b128 v[8:11], v125 offset:40960
	ds_read_b128 v[12:15], v125 offset:41984
	v_pk_fma_f32 v[2:3], v[100:101], v[6:7], v[2:3] op_sel_hi:[0,1,1]
	s_waitcnt lgkmcnt(1)
	v_fmac_f32_e32 v136, v101, v10
	v_fmac_f32_e32 v53, v101, v11
	s_waitcnt lgkmcnt(0)
	v_fmac_f32_e32 v51, v101, v12
	v_fmac_f32_e32 v49, v101, v13
	v_fmac_f32_e32 v47, v101, v14
	v_fmac_f32_e32 v45, v101, v15
	v_mov_b32_e32 v10, v216
	v_mov_b32_e32 v11, v217
	v_mov_b32_e32 v12, v218
	v_mov_b32_e32 v13, v219
	v_mov_b32_e32 v14, v220
	v_mov_b32_e32 v15, v221
	v_mov_b32_e32 v16, v222
	v_mov_b32_e32 v17, v223
	v_mov_b32_e32 v106, v224
	v_mov_b32_e32 v107, v225
	v_mov_b32_e32 v108, v226
	v_mov_b32_e32 v109, v227
	v_pk_fma_f32 v[2:3], v[100:101], v[8:9], v[2:3] op_sel:[1,0,0]
	v_pk_mul_f32 v[10:11], v[18:19], v[10:11]
	v_pk_mul_f32 v[12:13], v[110:111], v[12:13]
	v_pk_add_f32 v[106:107], v[106:107], 1.0 op_sel_hi:[1,0]
	v_pk_add_f32 v[18:19], v[108:109], 1.0 op_sel_hi:[1,0]
	v_pk_fma_f32 v[106:107], v[10:11], v[106:107], v[14:15]
	v_mov_b32_e32 v14, 0
	v_med3_f32 v10, v106, s51, v133
	v_med3_f32 v11, v107, s51, v133
	v_cvt_pk_fp8_f32 v14, v10, v11
	v_pk_fma_f32 v[98:99], v[12:13], v[18:19], v[16:17]
	s_nop 0
	v_med3_f32 v12, v98, s51, v133
	v_med3_f32 v13, v99, s51, v133
	v_cvt_pk_fp8_f32 v14, v12, v13 op_sel:[0,0,1]
	global_store_dword v[86:87], v14, off offset:1280
	ds_read_b128 v[10:13], v125 offset:43008
	ds_read_b128 v[14:17], v125 offset:44032
	s_waitcnt lgkmcnt(1)
	v_fmac_f32_e32 v136, v106, v12
	v_fmac_f32_e32 v53, v106, v13
	s_waitcnt lgkmcnt(0)
	v_fmac_f32_e32 v51, v106, v14
	v_fmac_f32_e32 v49, v106, v15
	v_fmac_f32_e32 v47, v106, v16
	v_fmac_f32_e32 v45, v106, v17
	ds_read_b128 v[12:15], v125 offset:45056
	ds_read_b128 v[16:19], v125 offset:46080
	v_pk_fma_f32 v[2:3], v[106:107], v[10:11], v[2:3] op_sel_hi:[0,1,1]
	s_waitcnt lgkmcnt(1)
	v_fmac_f32_e32 v136, v107, v14
	v_fmac_f32_e32 v53, v107, v15
	s_waitcnt lgkmcnt(0)
	v_fmac_f32_e32 v51, v107, v16
	v_fmac_f32_e32 v49, v107, v17
	ds_read_b128 v[14:17], v125 offset:47104
	ds_read_b128 v[108:111], v125 offset:48128
	v_fmac_f32_e32 v47, v107, v18
	v_fmac_f32_e32 v45, v107, v19
	v_pk_fma_f32 v[2:3], v[106:107], v[12:13], v[2:3] op_sel:[1,0,0]
	s_waitcnt lgkmcnt(1)
	v_fmac_f32_e32 v136, v98, v16
	v_fmac_f32_e32 v53, v98, v17
	s_waitcnt lgkmcnt(0)
	v_fmac_f32_e32 v51, v98, v108
	v_fmac_f32_e32 v49, v98, v109
	v_fmac_f32_e32 v47, v98, v110
	v_fmac_f32_e32 v45, v98, v111
	ds_read_b128 v[16:19], v125 offset:49152
	ds_read_b128 v[108:111], v125 offset:50176
	v_pk_fma_f32 v[2:3], v[98:99], v[14:15], v[2:3] op_sel_hi:[0,1,1]
	s_waitcnt lgkmcnt(1)
	v_fmac_f32_e32 v136, v99, v18
	s_waitcnt lgkmcnt(0)
	v_fmac_f32_e32 v51, v99, v108
	v_fmac_f32_e32 v49, v99, v109
	v_fmac_f32_e32 v47, v99, v110
	v_fmac_f32_e32 v45, v99, v111
	v_mov_b32_e32 v108, v228
	v_mov_b32_e32 v109, v229
	v_mov_b32_e32 v110, v230
	v_mov_b32_e32 v111, v231
	v_mov_b32_e32 v112, v232
	v_mov_b32_e32 v113, v233
	v_mov_b32_e32 v114, v234
	v_mov_b32_e32 v115, v235
	v_mov_b32_e32 v116, v236
	v_mov_b32_e32 v117, v237
	v_mov_b32_e32 v118, v238
	v_mov_b32_e32 v119, v239
	v_fmac_f32_e32 v53, v99, v19
	v_pk_mul_f32 v[18:19], v[90:91], v[96:97] op_sel_hi:[0,1]
	v_pk_fma_f32 v[2:3], v[98:99], v[16:17], v[2:3] op_sel:[1,0,0]
	v_pk_mul_f32 v[94:95], v[94:95], v[108:109]
	v_pk_mul_f32 v[18:19], v[18:19], v[110:111]
	v_pk_add_f32 v[108:109], v[116:117], 1.0 op_sel_hi:[1,0]
	v_pk_add_f32 v[96:97], v[118:119], 1.0 op_sel_hi:[1,0]
	v_pk_fma_f32 v[94:95], v[94:95], v[108:109], v[112:113]
	v_pk_fma_f32 v[18:19], v[18:19], v[96:97], v[114:115]
	v_med3_f32 v88, v94, s51, v133
	v_med3_f32 v96, v95, s51, v133
	v_mov_b32_e32 v109, 0
	v_cvt_pk_fp8_f32 v109, v88, v96
	v_med3_f32 v97, v18, s51, v133
	v_med3_f32 v108, v19, s51, v133
	v_mov_b32_e32 v88, v91
	v_cvt_pk_fp8_f32 v109, v97, v108 op_sel:[0,0,1]
	v_pk_mul_f32 v[88:89], v[88:89], v[90:91] op_sel_hi:[1,0]
	global_store_dword v[86:87], v109, off offset:1536
	ds_read_b128 v[108:111], v125 offset:51200
	ds_read_b128 v[112:115], v125 offset:52224
	s_waitcnt lgkmcnt(1)
; #define GAS __attribute__((address_space(1)))
; __device__ __forceinline__ unsigned pk4_fp8(float a, float b, float c, float d) { int p = 0; p = __builtin_amdgcn_cvt_pk_fp8_f32(a, b, p, false); p = __builtin_amdgcn_cvt_pk_fp8_f32(c, d, p, true); return (unsigned)p; }
; __device__ __forceinline__ float clamp8(float x) { return __builtin_fminf(__builtin_fmaxf(x, -448.0f), 448.0f); }
; __device__ __forceinline__ float wave_sum(float v) {
; #pragma unroll
;     for (int o = 1; o < 64; o <<= 1) v += __shfl_xor(v, o);
;     return v;
; __device__ __forceinline__ void route_phase(Frame& F) {
;     ...
;             for (int j = 0; j < 8; ++j) { const int col = 4 * (F.lane + 64 * j);
;                 const f32x4 gg = *(const GAS f32x4*)(g + col), sh = *(const GAS f32x4*)(mv + 3 * DM + col), sc = *(const GAS f32x4*)(mv + 4 * DM + col);
;                 const f32x4 y = v[j] * rstd * gg * (sc + 1.0f) + sh; o4[64 * j] = pk4_fp8(clamp8(y.x), clamp8(y.y), clamp8(y.z), clamp8(y.w));
; #pragma unroll
;                 for (int q = 0; q < 4; ++q) { const f32x4 w0 = rwl[((j * 4 + q) * 2 + 0) * 64 + F.lane], w1 = rwl[((j * 4 + q) * 2 + 1) * 64 + F.lane];
;                     lg[0] += y[q] * w0.x; lg[1] += y[q] * w0.y; lg[2] += y[q] * w0.z; lg[3] += y[q] * w0.w; lg[4] += y[q] * w1.x; lg[5] += y[q] * w1.y; lg[6] += y[q] * w1.z; lg[7] += y[q] * w1.w; } }
; #pragma unroll
;             for (int e = 0; e < 8; ++e) lg[e] = wave_sum(lg[e]) + rb[e];
	v_fmac_f32_e32 v136, v94, v110
	v_fmac_f32_e32 v53, v94, v111
	s_waitcnt lgkmcnt(0)
	v_fmac_f32_e32 v51, v94, v112
	v_fmac_f32_e32 v49, v94, v113
	v_fmac_f32_e32 v47, v94, v114
	v_fmac_f32_e32 v45, v94, v115
	ds_read_b128 v[110:113], v125 offset:53248
	ds_read_b128 v[114:117], v125 offset:54272
	v_pk_fma_f32 v[2:3], v[94:95], v[108:109], v[2:3] op_sel_hi:[0,1,1]
	s_waitcnt lgkmcnt(1)
	v_fmac_f32_e32 v136, v95, v112
	v_fmac_f32_e32 v53, v95, v113
	s_waitcnt lgkmcnt(0)
	v_fmac_f32_e32 v51, v95, v114
	v_fmac_f32_e32 v49, v95, v115
	v_fmac_f32_e32 v47, v95, v116
	v_fmac_f32_e32 v45, v95, v117
	ds_read_b128 v[112:115], v125 offset:55296
	ds_read_b128 v[116:119], v125 offset:56320
	v_pk_fma_f32 v[2:3], v[94:95], v[110:111], v[2:3] op_sel:[1,0,0]
	s_waitcnt lgkmcnt(1)
	v_fmac_f32_e32 v136, v18, v114
	v_pk_fma_f32 v[16:17], v[18:19], v[112:113], v[2:3] op_sel_hi:[0,1,1]
	ds_read_b128 v[2:5], v125 offset:57344
	ds_read_b128 v[6:9], v125 offset:58368
	v_fmac_f32_e32 v53, v18, v115
	s_waitcnt lgkmcnt(2)
	v_fmac_f32_e32 v51, v18, v116
	v_fmac_f32_e32 v49, v18, v117
	v_fmac_f32_e32 v47, v18, v118
	v_fmac_f32_e32 v45, v18, v119
	s_waitcnt lgkmcnt(1)
	v_fmac_f32_e32 v136, v19, v4
	v_fmac_f32_e32 v53, v19, v5
	s_waitcnt lgkmcnt(0)
	v_fmac_f32_e32 v51, v19, v6
	v_fmac_f32_e32 v49, v19, v7
	v_fmac_f32_e32 v47, v19, v8
	v_fmac_f32_e32 v45, v19, v9
	v_mov_b32_e32 v4, v240
	v_mov_b32_e32 v5, v241
	v_mov_b32_e32 v6, v242
	v_mov_b32_e32 v7, v243
	v_mov_b32_e32 v8, v244
	v_mov_b32_e32 v9, v245
	v_mov_b32_e32 v10, v246
	v_mov_b32_e32 v11, v247
	v_mov_b32_e32 v12, v252
	v_mov_b32_e32 v13, v253
	v_mov_b32_e32 v14, v254
	v_mov_b32_e32 v15, v255
	v_pk_fma_f32 v[2:3], v[18:19], v[2:3], v[16:17] op_sel:[1,0,0]
	v_pk_mul_f32 v[4:5], v[88:89], v[4:5]
	v_pk_mul_f32 v[6:7], v[92:93], v[6:7]
	v_pk_add_f32 v[12:13], v[12:13], 1.0 op_sel_hi:[1,0]
	v_pk_add_f32 v[14:15], v[14:15], 1.0 op_sel_hi:[1,0]
	v_pk_fma_f32 v[88:89], v[4:5], v[12:13], v[8:9]
	v_mov_b32_e32 v8, 0
	v_med3_f32 v4, v88, s51, v133
	v_med3_f32 v5, v89, s51, v133
	v_cvt_pk_fp8_f32 v8, v4, v5
	v_pk_fma_f32 v[14:15], v[6:7], v[14:15], v[10:11]
	s_nop 0
	v_med3_f32 v6, v14, s51, v133
	v_med3_f32 v7, v15, s51, v133
	v_cvt_pk_fp8_f32 v8, v6, v7 op_sel:[0,0,1]
	global_store_dword v[86:87], v8, off offset:1792
	ds_read_b128 v[4:7], v125 offset:59392
	ds_read_b128 v[8:11], v125 offset:60416
	s_waitcnt lgkmcnt(1)
	v_fmac_f32_e32 v136, v88, v6
	v_fmac_f32_e32 v53, v88, v7
	s_waitcnt lgkmcnt(0)
	v_fmac_f32_e32 v51, v88, v8
	v_fmac_f32_e32 v49, v88, v9
	v_fmac_f32_e32 v47, v88, v10
	v_fmac_f32_e32 v45, v88, v11
	ds_read_b128 v[6:9], v125 offset:61440
	ds_read_b128 v[10:13], v125 offset:62464
	v_pk_fma_f32 v[2:3], v[88:89], v[4:5], v[2:3] op_sel_hi:[0,1,1]
	s_waitcnt lgkmcnt(1)
	v_fmac_f32_e32 v136, v89, v8
	v_fmac_f32_e32 v53, v89, v9
	s_waitcnt lgkmcnt(0)
	v_fmac_f32_e32 v51, v89, v10
	v_fmac_f32_e32 v49, v89, v11
	ds_read_b128 v[8:11], v125 offset:63488
	ds_read_b128 v[90:93], v125 offset:64512
	v_fmac_f32_e32 v47, v89, v12
	v_fmac_f32_e32 v45, v89, v13
	v_pk_fma_f32 v[2:3], v[88:89], v[6:7], v[2:3] op_sel:[1,0,0]
	s_waitcnt lgkmcnt(1)
	v_fmac_f32_e32 v136, v14, v10
	v_fmac_f32_e32 v53, v14, v11
	s_waitcnt lgkmcnt(0)
	v_fmac_f32_e32 v51, v14, v90
	v_fmac_f32_e32 v49, v14, v91
	v_fmac_f32_e32 v47, v14, v92
	v_fmac_f32_e32 v45, v14, v93
	ds_read_b128 v[10:13], v126
	ds_read_b128 v[90:93], v127
	v_pk_fma_f32 v[2:3], v[14:15], v[8:9], v[2:3] op_sel_hi:[0,1,1]
	s_waitcnt lgkmcnt(1)
	v_fmac_f32_e32 v136, v15, v12
	v_fmac_f32_e32 v53, v15, v13
	s_waitcnt lgkmcnt(0)
	v_fmac_f32_e32 v51, v15, v90
	v_fmac_f32_e32 v49, v15, v91
	v_fmac_f32_e32 v47, v15, v92
	v_fmac_f32_e32 v45, v15, v93
	v_pk_fma_f32 v[2:3], v[14:15], v[10:11], v[2:3] op_sel:[1,0,0]
	ds_bpermute_b32 v4, v1, v2
	ds_bpermute_b32 v5, v1, v3
	ds_bpermute_b32 v6, v1, v136
	ds_bpermute_b32 v8, v1, v53
	ds_bpermute_b32 v10, v1, v51
	ds_bpermute_b32 v12, v1, v49
	ds_bpermute_b32 v14, v1, v47
	ds_bpermute_b32 v16, v1, v45
	s_waitcnt lgkmcnt(6)
	v_pk_add_f32 v[2:3], v[2:3], v[4:5]
	s_waitcnt lgkmcnt(5)
	v_add_f32_e32 v6, v136, v6
	s_waitcnt lgkmcnt(4)
	v_add_f32_e32 v8, v53, v8
	s_waitcnt lgkmcnt(3)
	v_add_f32_e32 v10, v51, v10
	s_waitcnt lgkmcnt(2)
	v_add_f32_e32 v12, v49, v12
	s_waitcnt lgkmcnt(1)
	v_add_f32_e32 v14, v47, v14
	s_waitcnt lgkmcnt(0)
	v_add_f32_e32 v16, v45, v16
	ds_bpermute_b32 v4, v120, v2
	ds_bpermute_b32 v5, v120, v3
	ds_bpermute_b32 v7, v120, v6
	ds_bpermute_b32 v9, v120, v8
	ds_bpermute_b32 v11, v120, v10
	ds_bpermute_b32 v13, v120, v12
	ds_bpermute_b32 v15, v120, v14
	ds_bpermute_b32 v17, v120, v16
	s_waitcnt lgkmcnt(6)
	v_pk_add_f32 v[2:3], v[2:3], v[4:5]
	s_waitcnt lgkmcnt(5)
	v_add_f32_e32 v6, v6, v7
	s_waitcnt lgkmcnt(4)
	v_add_f32_e32 v8, v8, v9
	s_waitcnt lgkmcnt(3)
	v_add_f32_e32 v10, v10, v11
	s_waitcnt lgkmcnt(2)
	v_add_f32_e32 v12, v12, v13
	s_waitcnt lgkmcnt(1)
	v_add_f32_e32 v14, v14, v15
	s_waitcnt lgkmcnt(0)
	v_add_f32_e32 v16, v16, v17
	ds_bpermute_b32 v4, v121, v2
	ds_bpermute_b32 v5, v121, v3
	ds_bpermute_b32 v7, v121, v6
	ds_bpermute_b32 v9, v121, v8
	ds_bpermute_b32 v11, v121, v10
	ds_bpermute_b32 v13, v121, v12
	ds_bpermute_b32 v15, v121, v14
	ds_bpermute_b32 v17, v121, v16
	s_waitcnt lgkmcnt(6)
	v_pk_add_f32 v[2:3], v[2:3], v[4:5]
	s_waitcnt lgkmcnt(5)
	v_add_f32_e32 v6, v6, v7
	s_waitcnt lgkmcnt(4)
	v_add_f32_e32 v8, v8, v9
	s_waitcnt lgkmcnt(3)
	v_add_f32_e32 v10, v10, v11
	s_waitcnt lgkmcnt(2)
	v_add_f32_e32 v12, v12, v13
	s_waitcnt lgkmcnt(1)
	v_add_f32_e32 v14, v14, v15
	s_waitcnt lgkmcnt(0)
; #define LAS __attribute__((address_space(3)))
; __device__ __forceinline__ void route_phase(Frame& F) {
;     ...
;             for (int e = 0; e < 8; ++e) lg[e] = wave_sum(lg[e]) + rb[e];
;             int e0 = 0; float l0 = lg[0];
; #pragma unroll
;             for (int e = 1; e < 8; ++e) if (lg[e] > l0) { l0 = lg[e]; e0 = e; }
;             int e1 = -1; float l1 = -3.0e38f;
; #pragma unroll
;             for (int e = 0; e < 8; ++e) if (e != e0 && lg[e] > l1) { l1 = lg[e]; e1 = e; }
;             if (F.lane == 0) { const float w1 = 1.0f / (1.0f + __expf(l0 - l1)); const int r0 = atomicAdd((int*)&lcnt[e0], 1), r1 = atomicAdd((int*)&lcnt[e1], 1);
;                 LAS int* pr = lrow + (F.wave * 8 + i) * 4; pr[0] = e0; pr[1] = r0; pr[2] = e1; pr[3] = r1;
;                 tok_e[2 * row] = e0; tok_e[2 * row + 1] = e1; tok_w[2 * row] = 1.0f - w1; tok_w[2 * row + 1] = w1; }
	v_add_f32_e32 v16, v16, v17
	ds_bpermute_b32 v4, v122, v2
	ds_bpermute_b32 v5, v122, v3
	ds_bpermute_b32 v7, v122, v6
	ds_bpermute_b32 v9, v122, v8
	ds_bpermute_b32 v11, v122, v10
	ds_bpermute_b32 v13, v122, v12
	ds_bpermute_b32 v15, v122, v14
	ds_bpermute_b32 v17, v122, v16
	s_waitcnt lgkmcnt(6)
	v_pk_add_f32 v[2:3], v[2:3], v[4:5]
	s_waitcnt lgkmcnt(5)
	v_add_f32_e32 v6, v6, v7
	s_waitcnt lgkmcnt(4)
	v_add_f32_e32 v8, v8, v9
	s_waitcnt lgkmcnt(3)
	v_add_f32_e32 v10, v10, v11
	s_waitcnt lgkmcnt(2)
	v_add_f32_e32 v12, v12, v13
	s_waitcnt lgkmcnt(1)
	v_add_f32_e32 v14, v14, v15
	s_waitcnt lgkmcnt(0)
	v_add_f32_e32 v16, v16, v17
	ds_bpermute_b32 v4, v123, v2
	ds_bpermute_b32 v5, v123, v3
	ds_bpermute_b32 v7, v123, v6
	ds_bpermute_b32 v9, v123, v8
	ds_bpermute_b32 v11, v123, v10
	ds_bpermute_b32 v13, v123, v12
	ds_bpermute_b32 v15, v123, v14
	ds_bpermute_b32 v17, v123, v16
	s_waitcnt lgkmcnt(6)
	v_pk_add_f32 v[2:3], v[2:3], v[4:5]
	s_waitcnt lgkmcnt(5)
	v_add_f32_e32 v6, v6, v7
	s_waitcnt lgkmcnt(4)
	v_add_f32_e32 v8, v8, v9
	s_waitcnt lgkmcnt(3)
	v_add_f32_e32 v10, v10, v11
	s_waitcnt lgkmcnt(2)
	v_add_f32_e32 v12, v12, v13
	s_waitcnt lgkmcnt(1)
	v_add_f32_e32 v14, v14, v15
	s_waitcnt lgkmcnt(0)
	v_add_f32_e32 v16, v16, v17
	ds_bpermute_b32 v4, v124, v2
	ds_bpermute_b32 v5, v124, v3
	ds_bpermute_b32 v7, v124, v6
	ds_bpermute_b32 v9, v124, v8
	ds_bpermute_b32 v11, v124, v10
	ds_bpermute_b32 v13, v124, v12
	ds_bpermute_b32 v15, v124, v14
	ds_bpermute_b32 v17, v124, v16
	s_and_saveexec_b64 s[34:35], s[4:5]
	s_cbranch_execz .LBB0_1745
	v_readlane_b32 s56, v250, 40
	v_readlane_b32 s68, v250, 52
	v_readlane_b32 s69, v250, 53
	s_nop 4
	global_load_dwordx4 v[86:89], v21, s[68:69] offset:16
	global_load_dwordx4 v[90:93], v21, s[68:69]
	s_waitcnt lgkmcnt(6)
	v_pk_add_f32 v[2:3], v[2:3], v[4:5]
	s_waitcnt lgkmcnt(5)
	v_add_f32_e32 v6, v6, v7
	s_waitcnt lgkmcnt(4)
	v_add_f32_e32 v8, v8, v9
	s_waitcnt lgkmcnt(3)
	v_add_f32_e32 v10, v10, v11
	s_waitcnt lgkmcnt(2)
	v_add_f32_e32 v12, v12, v13
	s_waitcnt lgkmcnt(1)
	v_add_f32_e32 v14, v14, v15
	s_waitcnt lgkmcnt(0)
	v_add_f32_e32 v16, v16, v17
	s_add_i32 s0, s46, s27
	v_mov_b32_e32 v7, s0
	v_readlane_b32 s57, v250, 41
	s_ashr_i32 s31, s30, 31
	s_lshl_b64 s[54:55], s[30:31], 2
	v_readlane_b32 s58, v250, 42
	v_readlane_b32 s59, v250, 43
	v_readlane_b32 s60, v250, 44
	v_readlane_b32 s61, v250, 45
	v_readlane_b32 s62, v250, 46
	v_readlane_b32 s63, v250, 47
	v_readlane_b32 s64, v250, 48
	v_readlane_b32 s65, v250, 49
	v_readlane_b32 s66, v250, 50
	v_readlane_b32 s67, v250, 51
	v_readlane_b32 s70, v250, 54
	v_readlane_b32 s71, v250, 55
	s_waitcnt vmcnt(1)
	v_add_f32_e32 v10, v10, v86
	s_waitcnt vmcnt(0)
	v_pk_add_f32 v[4:5], v[2:3], v[90:91]
	v_add_f32_e32 v6, v6, v92
	v_cmp_gt_f32_e32 vcc, v5, v4
	v_add_f32_e32 v8, v8, v93
	v_add_f32_e32 v12, v12, v87
	v_cndmask_b32_e32 v2, v4, v5, vcc
	v_cmp_gt_f32_e64 s[8:9], v6, v2
	v_cndmask_b32_e64 v3, 0, 1, vcc
	v_add_f32_e32 v11, v14, v88
	v_cndmask_b32_e64 v2, v2, v6, s[8:9]
	v_cmp_gt_f32_e32 vcc, v8, v2
	v_cndmask_b32_e64 v3, v3, 2, s[8:9]
	v_add_f32_e32 v9, v16, v89
	v_cndmask_b32_e32 v2, v2, v8, vcc
	v_cmp_gt_f32_e64 s[8:9], v10, v2
	v_cndmask_b32_e64 v3, v3, 3, vcc
	v_cmp_nlt_f32_e64 s[0:1], s52, v4
	v_cndmask_b32_e64 v2, v2, v10, s[8:9]
	v_cmp_gt_f32_e32 vcc, v12, v2
	v_cndmask_b32_e64 v3, v3, 4, s[8:9]
	s_nop 0
	v_cndmask_b32_e32 v2, v2, v12, vcc
	v_cmp_gt_f32_e64 s[8:9], v11, v2
	s_nop 1
	v_cndmask_b32_e64 v13, v2, v11, s[8:9]
	v_cndmask_b32_e64 v2, v3, 5, vcc
	v_cndmask_b32_e64 v2, v2, 6, s[8:9]
	v_cmp_ngt_f32_e32 vcc, v9, v13
	s_and_b64 s[56:57], s[8:9], vcc
	s_nop 0
	v_cndmask_b32_e32 v2, 7, v2, vcc
	v_cmp_eq_u32_e64 s[18:19], 0, v2
	s_or_b64 s[0:1], s[18:19], s[0:1]
	v_cndmask_b32_e64 v4, v4, v134, s[0:1]
	v_cmp_ne_u32_e64 s[16:17], 1, v2
	v_cmp_gt_f32_e64 s[18:19], v5, v4
	v_cndmask_b32_e64 v14, 0, -1, s[0:1]
	s_and_b64 s[0:1], s[16:17], s[18:19]
	v_cndmask_b32_e64 v4, v4, v5, s[0:1]
	v_cmp_ne_u32_e64 s[14:15], 2, v2
	v_cmp_gt_f32_e64 s[16:17], v6, v4
	v_cndmask_b32_e64 v5, v14, 1, s[0:1]
	s_and_b64 s[0:1], s[14:15], s[16:17]
	v_cndmask_b32_e64 v4, v4, v6, s[0:1]
	v_cmp_ne_u32_e64 s[12:13], 3, v2
	v_cmp_gt_f32_e64 s[14:15], v8, v4
	v_cndmask_b32_e64 v5, v5, 2, s[0:1]
	s_and_b64 s[0:1], s[12:13], s[14:15]
	v_cndmask_b32_e64 v4, v4, v8, s[0:1]
	v_cmp_ne_u32_e64 s[10:11], 4, v2
	v_cmp_gt_f32_e64 s[12:13], v10, v4
	v_cndmask_b32_e64 v5, v5, 3, s[0:1]
	s_and_b64 s[0:1], s[10:11], s[12:13]
	v_cndmask_b32_e64 v4, v4, v10, s[0:1]
	v_cmp_ne_u32_e64 s[8:9], 5, v2
	v_cmp_gt_f32_e64 s[10:11], v12, v4
	v_cndmask_b32_e64 v5, v5, 4, s[0:1]
	s_and_b64 s[0:1], s[8:9], s[10:11]
	v_cndmask_b32_e64 v4, v4, v12, s[0:1]
	v_cmp_ngt_f32_e64 s[8:9], v11, v4
	v_cndmask_b32_e64 v5, v5, 5, s[0:1]
	s_or_b64 s[0:1], s[56:57], s[8:9]
	v_cndmask_b32_e64 v6, v11, v4, s[0:1]
	v_cmp_gt_f32_e64 s[8:9], v9, v6
	v_cndmask_b32_e32 v13, v9, v13, vcc
	v_cndmask_b32_e64 v4, 6, v5, s[0:1]
	s_and_b64 vcc, vcc, s[8:9]
	v_lshl_add_u32 v3, v2, 2, 0
	v_cndmask_b32_e64 v4, v4, 7, vcc
	v_cndmask_b32_e32 v5, v6, v9, vcc
	ds_add_rtn_u32 v3, v3, v135
	v_lshl_add_u32 v6, v4, 2, 0
	v_sub_f32_e32 v8, v13, v5
	ds_add_rtn_u32 v5, v6, v135
	v_mul_f32_e32 v6, 0x3fb8aa3b, v8
	v_exp_f32_e32 v6, v6
	s_add_u32 s0, s38, s54
	s_addc_u32 s1, s39, s55
	s_waitcnt lgkmcnt(0)
	ds_write_b128 v7, v[2:5]
	v_mov_b32_e32 v3, v4
	v_add_f32_e32 v4, 1.0, v6
	v_div_scale_f32 v5, s[12:13], v4, v4, 1.0
	v_rcp_f32_e32 v6, v5
	global_store_dwordx2 v21, v[2:3], s[0:1]
	v_div_scale_f32 v2, vcc, 1.0, v4, 1.0
	v_fma_f32 v3, -v5, v6, 1.0
	v_fmac_f32_e32 v6, v3, v6
	v_mul_f32_e32 v3, v2, v6
	v_fma_f32 v7, -v5, v3, v2
	s_add_i32 s8, s30, 1
	v_fmac_f32_e32 v3, v7, v6
	s_ashr_i32 s9, s8, 31
	v_fma_f32 v2, -v5, v3, v2
	s_add_u32 s10, s40, s54
	v_div_fmas_f32 v2, v2, v6, v3
	s_addc_u32 s11, s41, s55
	s_lshl_b64 s[8:9], s[8:9], 2
	v_div_fixup_f32 v2, v2, v4, 1.0
	s_add_u32 s8, s40, s8
	v_sub_f32_e32 v3, 1.0, v2
	s_addc_u32 s9, s41, s9
	global_store_dword v21, v3, s[10:11]
	global_store_dword v21, v2, s[8:9]
	s_branch .LBB0_1745

; __global__ void __launch_bounds__(NWAVES * 64, 2) fwd_kernel(Args args) {
	.amdhsa_kernel _Z10fwd_kernel4Args
		.amdhsa_group_segment_fixed_size 0
		.amdhsa_private_segment_fixed_size 0
		.amdhsa_kernarg_size 560
		.amdhsa_user_sgpr_count 2
		.amdhsa_user_sgpr_dispatch_ptr 0
		.amdhsa_user_sgpr_queue_ptr 0
		.amdhsa_user_sgpr_kernarg_segment_ptr 1
		.amdhsa_user_sgpr_dispatch_id 0
		.amdhsa_user_sgpr_kernarg_preload_length 0
		.amdhsa_user_sgpr_kernarg_preload_offset 0
		.amdhsa_user_sgpr_private_segment_size 0
		.amdhsa_uses_dynamic_stack 0
		.amdhsa_enable_private_segment 0
		.amdhsa_system_sgpr_workgroup_id_x 1
		.amdhsa_system_sgpr_workgroup_id_y 0
		.amdhsa_system_sgpr_workgroup_id_z 0
		.amdhsa_system_sgpr_workgroup_info 0
		.amdhsa_system_vgpr_workitem_id 0
		.amdhsa_next_free_vgpr 256
		.amdhsa_next_free_sgpr 102
		.amdhsa_accum_offset 256
		.amdhsa_reserve_vcc 1
		.amdhsa_float_round_mode_32 0
		.amdhsa_float_round_mode_16_64 0
		.amdhsa_float_denorm_mode_32 3
		.amdhsa_float_denorm_mode_16_64 3
		.amdhsa_dx10_clamp 1
		.amdhsa_ieee_mode 1
		.amdhsa_fp16_overflow 0
		.amdhsa_tg_split 0
		.amdhsa_exception_fp_ieee_invalid_op 0
		.amdhsa_exception_fp_denorm_src 0
		.amdhsa_exception_fp_ieee_div_zero 0
		.amdhsa_exception_fp_ieee_overflow 0
		.amdhsa_exception_fp_ieee_underflow 0
		.amdhsa_exception_fp_ieee_inexact 0
		.amdhsa_exception_int_div_zero 0
	.end_amdhsa_kernel

; __global__ void __launch_bounds__(NWAVES * 64, 2) fwd_kernel(Args args) {
amdhsa.kernels:
  - .agpr_count:     0
    .args:
      - .offset:         0
        .size:           304
        .value_kind:     by_value
      - .offset:         304
        .size:           4
        .value_kind:     hidden_block_count_x
      - .offset:         308
        .size:           4
        .value_kind:     hidden_block_count_y
      - .offset:         312
        .size:           4
        .value_kind:     hidden_block_count_z
      - .offset:         316
        .size:           2
        .value_kind:     hidden_group_size_x
      - .offset:         318
        .size:           2
        .value_kind:     hidden_group_size_y
      - .offset:         320
        .size:           2
        .value_kind:     hidden_group_size_z
      - .offset:         322
        .size:           2
        .value_kind:     hidden_remainder_x
      - .offset:         324
        .size:           2
        .value_kind:     hidden_remainder_y
      - .offset:         326
        .size:           2
        .value_kind:     hidden_remainder_z
      - .offset:         344
        .size:           8
        .value_kind:     hidden_global_offset_x
      - .offset:         352
        .size:           8
        .value_kind:     hidden_global_offset_y
      - .offset:         360
        .size:           8
        .value_kind:     hidden_global_offset_z
      - .offset:         368
        .size:           2
        .value_kind:     hidden_grid_dims
      - .offset:         424
        .size:           4
        .value_kind:     hidden_dynamic_lds_size
    .group_segment_fixed_size: 0
    .kernarg_segment_align: 8
    .kernarg_segment_size: 560
    .language:       OpenCL C
    .language_version:
      - 2
      - 0
    .max_flat_workgroup_size: 512
    .name:           _Z10fwd_kernel4Args
    .private_segment_fixed_size: 0
    .sgpr_count:     108
    .sgpr_spill_count: 162
    .symbol:         _Z10fwd_kernel4Args.kd
    .uniform_work_group_size: 1
    .uses_dynamic_stack: false
    .vgpr_count:     256
    .vgpr_spill_count: 0
    .wavefront_size: 64
